# baseline (speedup 1.0000x reference)
.LBB3_6:
	s_mov_b32 s2, s40
	s_add_i32 s40, s40, 1
	s_mov_b32 s41, s12
	s_lshl_b32 s12, s40, 5
	s_cmp_eq_u32 s2, 7
	s_cselect_b64 s[2:3], -1, 0
	s_and_b64 s[16:17], s[2:3], exec
	s_cselect_b32 s12, 0xe0, s12
	s_add_i32 s16, s12, s18
	s_lshr_b32 s12, s16, 4
	s_and_b32 s12, s12, 0xfffff8
	s_lshl_b32 s16, s16, 5
	s_mov_b32 s42, s35
	s_or_b32 s12, s12, s19
	s_and_b32 s35, s16, 0xf00
	s_lshl_b32 s16, s40, 10
	s_lshl_b32 s12, s12, 8
	s_and_b32 s43, s16, 0x400
	s_or_b64 s[2:3], vcc, s[2:3]
	s_lshl_b32 s44, s41, 7
	v_lshl_add_u64 v[202:203], s[12:13], 2, v[196:197]
	s_mov_b32 s45, 0x404000
	s_xor_b64 s[2:3], s[2:3], -1
	v_add_u32_e32 v194, s43, v208
	s_mov_b32 s46, 0
	.p2align	6

.LBB4_14:
	s_add_i32 s37, s37, 2
	s_add_i32 s2, s2, 0x40000
	s_cmpk_gt_u32 s40, 0x81
	v_add_u32_e32 v137, 32, v137
	s_cbranch_scc1 .LBB4_18
	.p2align	6
